# norm_kvq phase: first row tile loads issued in front of the per-workgroup weight-table build (into dead registers, copied into place afterwards); on top of v62
# baseline (speedup 1.0000x reference)
.LBB0_1209:
	v_readlane_b32 s60, v253, 18
	v_lshlrev_b32_e32 v2, 2, v0
	v_mov_b32_e32 v3, 0
	v_readlane_b32 s61, v253, 19
	v_readlane_b32 s62, v253, 20
	v_readlane_b32 s63, v253, 21
	s_waitcnt vmcnt(0)
	v_lshl_add_u64 v[6:7], s[60:61], 0, v[2:3]
	s_movk_i32 s4, 0x2040
	v_mov_b64_e32 v[2:3], s[62:63]
	v_mad_u64_u32 v[2:3], s[4:5], v0, s4, v[2:3]
	s_mov_b64 s[4:5], 0x2000
	v_or_b32_e32 v1, 0xfffffe00, v0
	v_lshl_add_u32 v10, v0, 1, 0
	v_lshl_add_u64 v[8:9], v[2:3], 0, s[4:5]
	s_mov_b64 s[4:5], 0
	s_movk_i32 s14, 0x7fff
	s_mov_b64 s[6:7], 0x800
	s_mov_b64 s[8:9], 0x408000
	v_readlane_b32 s64, v253, 22
	v_readlane_b32 s65, v253, 23
	v_readlane_b32 s66, v253, 24
	v_readlane_b32 s67, v253, 25
	v_readlane_b32 s68, v253, 26
	v_readlane_b32 s69, v253, 27
	v_readlane_b32 s70, v253, 28
	v_readlane_b32 s71, v253, 29
	v_readlane_b32 s72, v253, 30
	v_readlane_b32 s73, v253, 31
	v_readlane_b32 s74, v253, 32
	v_readlane_b32 s75, v253, 33
	s_lshl_b32 s16, s95, 6
	v_or_b32_e32 v120, s16, v222
	v_ashrrev_i32_e32 v121, 31, v120
	v_lshlrev_b64 v[120:121], 11, v[120:121]
	v_lshl_add_u64 v[120:121], s[2:3], 0, v[120:121]
	v_and_b32_e32 v122, 48, v0
	v_lshl_or_b32 v122, s92, 8, v122
	v_mov_b32_e32 v123, 0
	v_lshl_add_u64 v[120:121], v[120:121], 0, v[122:123]
	v_bfe_u32 v122, v0, 2, 4
	v_lshlrev_b32_e32 v122, 2, v122
	global_load_dword v100, v122, s[64:65]
	global_load_dwordx4 v[102:105], v[120:121], off
	global_load_dwordx4 v[106:109], v[120:121], off offset:64
	global_load_dwordx4 v[110:113], v[120:121], off offset:128
	global_load_dwordx4 v[114:117], v[120:121], off offset:192
.LBB0_1210:
	global_load_dword v11, v[6:7], off
	global_load_dwordx4 v[12:15], v[8:9], off
	global_load_dwordx4 v[16:19], v[8:9], off offset:16
	global_load_dwordx4 v[20:23], v[8:9], off offset:32
	global_load_dwordx4 v[2:5], v[8:9], off offset:48
	v_add_co_u32_e32 v1, vcc, 0x200, v1
	s_xor_b64 s[16:17], vcc, -1
	s_and_b64 s[16:17], exec, s[16:17]
	v_lshl_add_u64 v[6:7], v[6:7], 0, s[6:7]
	v_lshl_add_u64 v[8:9], v[8:9], 0, s[8:9]
	s_or_b64 s[4:5], s[16:17], s[4:5]
	s_waitcnt vmcnt(0)
	v_mul_f32_e32 v24, v11, v12
	v_mul_f32_e32 v25, v11, v13
	v_mul_f32_e32 v26, v11, v14
	v_mul_f32_e32 v27, v11, v15
	v_mul_f32_e32 v28, v11, v16
	v_mul_f32_e32 v29, v11, v17
	v_mul_f32_e32 v30, v11, v18
	v_mul_f32_e32 v31, v11, v19
	v_mul_f32_e32 v32, v11, v20
	v_mul_f32_e32 v33, v11, v21
	v_mul_f32_e32 v34, v11, v22
	v_mul_f32_e32 v35, v11, v23
	v_mul_f32_e32 v36, v11, v2
	v_mul_f32_e32 v37, v11, v3
	v_mul_f32_e32 v38, v11, v4
	v_mul_f32_e32 v39, v11, v5
	v_bfe_u32 v40, v24, 16, 1
	v_bfe_u32 v41, v25, 16, 1
	v_bfe_u32 v42, v26, 16, 1
	v_bfe_u32 v43, v27, 16, 1
	v_bfe_u32 v44, v28, 16, 1
	v_bfe_u32 v45, v29, 16, 1
	v_bfe_u32 v46, v30, 16, 1
	v_bfe_u32 v47, v31, 16, 1
	v_bfe_u32 v48, v32, 16, 1
	v_bfe_u32 v49, v33, 16, 1
	v_bfe_u32 v50, v34, 16, 1
	v_bfe_u32 v51, v35, 16, 1
	v_bfe_u32 v52, v36, 16, 1
	v_bfe_u32 v53, v37, 16, 1
	v_bfe_u32 v54, v38, 16, 1
	v_bfe_u32 v55, v39, 16, 1
	v_add3_u32 v24, v24, v40, s14
	v_add3_u32 v25, v25, v41, s14
	v_add3_u32 v26, v26, v42, s14
	v_add3_u32 v27, v27, v43, s14
	v_add3_u32 v28, v28, v44, s14
	v_add3_u32 v29, v29, v45, s14
	v_add3_u32 v30, v30, v46, s14
	v_add3_u32 v31, v31, v47, s14
	v_add3_u32 v32, v32, v48, s14
	v_add3_u32 v33, v33, v49, s14
	v_add3_u32 v34, v34, v50, s14
	v_add3_u32 v35, v35, v51, s14
	v_add3_u32 v36, v36, v52, s14
	v_add3_u32 v37, v37, v53, s14
	v_add3_u32 v38, v38, v54, s14
	v_add3_u32 v39, v39, v55, s14
	ds_write_b16_d16_hi v10, v24
	v_and_b32_e32 v24, 0xffff0000, v24
	ds_write_b16_d16_hi v10, v25 offset:2048
	v_and_b32_e32 v25, 0xffff0000, v25
	ds_write_b16_d16_hi v10, v26 offset:4096
	v_and_b32_e32 v26, 0xffff0000, v26
	ds_write_b16_d16_hi v10, v27 offset:6144
	v_and_b32_e32 v27, 0xffff0000, v27
	ds_write_b16_d16_hi v10, v28 offset:8192
	v_and_b32_e32 v28, 0xffff0000, v28
	ds_write_b16_d16_hi v10, v29 offset:10240
	v_and_b32_e32 v29, 0xffff0000, v29
	ds_write_b16_d16_hi v10, v30 offset:12288
	v_and_b32_e32 v30, 0xffff0000, v30
	ds_write_b16_d16_hi v10, v31 offset:14336
	v_and_b32_e32 v31, 0xffff0000, v31
	ds_write_b16_d16_hi v10, v32 offset:16384
	v_and_b32_e32 v32, 0xffff0000, v32
	ds_write_b16_d16_hi v10, v33 offset:18432
	v_and_b32_e32 v33, 0xffff0000, v33
	ds_write_b16_d16_hi v10, v34 offset:20480
	v_and_b32_e32 v34, 0xffff0000, v34
	ds_write_b16_d16_hi v10, v35 offset:22528
	v_and_b32_e32 v35, 0xffff0000, v35
	ds_write_b16_d16_hi v10, v36 offset:24576
	v_and_b32_e32 v36, 0xffff0000, v36
	ds_write_b16_d16_hi v10, v37 offset:26624
	v_and_b32_e32 v37, 0xffff0000, v37
	ds_write_b16_d16_hi v10, v38 offset:28672
	v_and_b32_e32 v38, 0xffff0000, v38
	ds_write_b16_d16_hi v10, v39 offset:30720
	v_and_b32_e32 v39, 0xffff0000, v39
	v_fma_f32 v12, v11, v12, -v24
	v_fma_f32 v13, v11, v13, -v25
	v_fma_f32 v14, v11, v14, -v26
	v_fma_f32 v15, v11, v15, -v27
	v_fma_f32 v16, v11, v16, -v28
	v_fma_f32 v17, v11, v17, -v29
	v_fma_f32 v18, v11, v18, -v30
	v_fma_f32 v19, v11, v19, -v31
	v_fma_f32 v20, v11, v20, -v32
	v_fma_f32 v21, v11, v21, -v33
	v_fma_f32 v22, v11, v22, -v34
	v_fma_f32 v23, v11, v23, -v35
	v_fma_f32 v2, v11, v2, -v36
	v_fma_f32 v3, v11, v3, -v37
	v_fma_f32 v4, v11, v4, -v38
	v_fma_f32 v5, v11, v5, -v39
	v_bfe_u32 v11, v12, 16, 1
	v_bfe_u32 v24, v13, 16, 1
	v_bfe_u32 v25, v14, 16, 1
	v_bfe_u32 v26, v15, 16, 1
	v_bfe_u32 v27, v16, 16, 1
	v_bfe_u32 v28, v17, 16, 1
	v_bfe_u32 v29, v18, 16, 1
	v_bfe_u32 v30, v19, 16, 1
	v_bfe_u32 v31, v20, 16, 1
	v_bfe_u32 v32, v21, 16, 1
	v_bfe_u32 v33, v22, 16, 1
	v_bfe_u32 v34, v23, 16, 1
	v_bfe_u32 v35, v2, 16, 1
	v_bfe_u32 v36, v3, 16, 1
	v_bfe_u32 v37, v4, 16, 1
	v_bfe_u32 v38, v5, 16, 1
	v_add3_u32 v11, v12, v11, s14
	v_add3_u32 v12, v13, v24, s14
	v_add3_u32 v13, v14, v25, s14
	v_add3_u32 v14, v15, v26, s14
	v_add3_u32 v15, v16, v27, s14
	v_add3_u32 v16, v17, v28, s14
	v_add3_u32 v17, v18, v29, s14
	v_add3_u32 v18, v19, v30, s14
	v_add3_u32 v19, v20, v31, s14
	v_add3_u32 v20, v21, v32, s14
	v_add3_u32 v21, v22, v33, s14
	v_add3_u32 v22, v23, v34, s14
	v_add3_u32 v2, v2, v35, s14
	v_add3_u32 v3, v3, v36, s14
	v_add3_u32 v4, v4, v37, s14
	v_add3_u32 v5, v5, v38, s14
	ds_write_b16_d16_hi v10, v11 offset:32768
	ds_write_b16_d16_hi v10, v12 offset:34816
	ds_write_b16_d16_hi v10, v13 offset:36864
	ds_write_b16_d16_hi v10, v14 offset:38912
	ds_write_b16_d16_hi v10, v15 offset:40960
	ds_write_b16_d16_hi v10, v16 offset:43008
	ds_write_b16_d16_hi v10, v17 offset:45056
	ds_write_b16_d16_hi v10, v18 offset:47104
	ds_write_b16_d16_hi v10, v19 offset:49152
	ds_write_b16_d16_hi v10, v20 offset:51200
	ds_write_b16_d16_hi v10, v21 offset:53248
	ds_write_b16_d16_hi v10, v22 offset:55296
	ds_write_b16_d16_hi v10, v2 offset:57344
	ds_write_b16_d16_hi v10, v3 offset:59392
	ds_write_b16_d16_hi v10, v4 offset:61440
	ds_write_b16_d16_hi v10, v5 offset:63488
	v_add_u32_e32 v10, 0x400, v10
	s_andn2_b64 exec, exec, s[4:5]
	s_cbranch_execnz .LBB0_1210
	s_or_b64 exec, exec, s[4:5]
	s_lshl_b32 s16, s95, 6
	v_or_b32_e32 v2, s16, v222
	v_ashrrev_i32_e32 v3, 31, v2
	v_lshlrev_b64 v[2:3], 11, v[2:3]
	v_and_b32_e32 v4, 48, v0
	v_bfe_u32 v20, v0, 2, 4
	v_readlane_b32 s60, v253, 18
	v_lshl_add_u64 v[2:3], s[2:3], 0, v[2:3]
	v_lshl_or_b32 v18, s92, 8, v4
	v_mov_b32_e32 v19, 0
	v_lshlrev_b32_e32 v1, 2, v20
	v_readlane_b32 s64, v253, 22
	v_readlane_b32 s65, v253, 23
	v_lshl_add_u64 v[14:15], v[2:3], 0, v[18:19]
	s_waitcnt lgkmcnt(0)
	s_barrier
	v_lshl_add_u64 v[34:35], s[2:3], 0, v[18:19]
	s_nop 0
	s_waitcnt vmcnt(0)
	v_mov_b32_e32 v1, v100
	v_mov_b64_e32 v[2:3], v[102:103]
	v_mov_b64_e32 v[4:5], v[104:105]
	v_mov_b64_e32 v[6:7], v[106:107]
	v_mov_b64_e32 v[8:9], v[108:109]
	v_mov_b64_e32 v[10:11], v[110:111]
	v_mov_b64_e32 v[12:13], v[112:113]
	v_mov_b64_e32 v[14:15], v[114:115]
	v_mov_b64_e32 v[16:17], v[116:117]
	s_nop 0
	s_nop 0
	v_mbcnt_hi_u32_b32 v19, -1, v227
	v_and_b32_e32 v22, 64, v19
	v_xor_b32_e32 v21, 16, v19
	v_add_u32_e32 v22, 64, v22
	v_cmp_lt_i32_e32 vcc, v21, v22
	s_cmp_eq_u32 s95, 0
	v_and_b32_e32 v44, 3, v0
	v_cndmask_b32_e32 v21, v19, v21, vcc
	v_lshlrev_b32_e32 v40, 2, v21
	v_xor_b32_e32 v21, 32, v19
	v_cmp_lt_i32_e32 vcc, v21, v22
	s_cselect_b32 s18, 5, 4
	s_and_b32 s4, s77, 0xffffffc0
	v_cndmask_b32_e32 v19, v19, v21, vcc
	v_lshlrev_b32_e32 v41, 2, v19
	v_lshlrev_b32_e32 v19, 11, v222
	s_add_i32 s6, 0, 0x10000
	v_and_or_b32 v45, v226, 12, v44
	v_add3_u32 v42, 0, v19, v18
	s_add_i32 s4, s6, s4
	v_lshl_add_u32 v46, v45, 2, s6
	s_mov_b32 s6, 0x10400
	v_mov_b64_e32 v[18:19], s[10:11]
	v_lshl_add_u32 v43, v208, 2, s4
	s_movk_i32 s4, 0x100
	v_and_b32_e32 v21, 0xfc, v0
	v_mad_u64_u32 v[36:37], s[6:7], v20, s6, v[18:19]
	s_mov_b32 s17, 0
	v_cmp_gt_u32_e32 vcc, 16, v208
	s_lshl_b32 s19, s92, 10
	v_cmp_gt_u32_e64 s[4:5], s4, v0
	v_cmp_eq_u32_e64 s[6:7], 0, v20
	v_lshlrev_b32_e32 v47, 2, v21
	v_mov_b32_e32 v48, 0x358637bd
	s_mov_b32 s20, 0x800000
	s_mov_b32 s21, 0xbfb8aa3b
	s_mov_b32 s22, 0xb2a5705f
	s_mov_b32 s23, 0x42ce8ed0
	s_mov_b32 s30, 0xc2b17218
	s_mov_b32 s31, 0x7f800000
	s_mov_b32 s34, 0x3f2aaaab
	v_mov_b32_e32 v49, 0x3ecc95a3
	s_mov_b32 s35, 0x3f317218
	s_mov_b32 s36, 0x33800000
	v_mov_b32_e32 v50, 0x7f800000
	v_mov_b32_e32 v38, 0x3f317218
	v_readlane_b32 s61, v253, 19
	v_readlane_b32 s62, v253, 20
	v_readlane_b32 s63, v253, 21
	v_readlane_b32 s66, v253, 24
	v_readlane_b32 s67, v253, 25
	v_readlane_b32 s68, v253, 26
	v_readlane_b32 s69, v253, 27
	v_readlane_b32 s70, v253, 28
	v_readlane_b32 s71, v253, 29
	v_readlane_b32 s72, v253, 30
	v_readlane_b32 s73, v253, 31
	v_readlane_b32 s74, v253, 32
	v_readlane_b32 s75, v253, 33
	s_branch .LBB0_1213
